# baseline (speedup 1.0000x reference)
.LBB1_3:
	s_mul_i32 s0, s7, s2
	s_sub_i32 s0, s6, s0
	s_add_i32 s1, s7, 1
	s_sub_i32 s6, s0, s2
	s_cmp_ge_u32 s0, s2
	s_cselect_b32 s1, s1, s7
	s_cselect_b32 s0, s6, s0
	s_add_i32 s6, s1, 1
	s_cmp_ge_u32 s0, s2
	s_cselect_b32 s0, s6, s1
	s_xor_b32 s0, s0, s5
	s_sub_i32 s0, s0, s5
	s_mul_i32 s79, s0, s76
	s_add_i32 s0, s79, s0
	s_lshl_b32 s33, s59, 7
	s_add_i32 s4, s33, s4
	s_min_i32 s80, s0, s3
	s_mul_i32 s0, s72, 0x4080
	s_mul_hi_i32 s1, s72, 0x4080
	s_add_u32 s0, s62, s0
	s_addc_u32 s1, s63, s1
	s_mul_i32 s2, s79, 0x4080
	v_and_b32_e32 v114, 63, v0
	s_mul_hi_i32 s3, s79, 0x4080
	s_add_u32 s2, s0, s2
	s_addc_u32 s3, s1, s3
	v_lshlrev_b32_e32 v108, 4, v114
	v_lshl_add_u64 v[2:3], s[2:3], 0, v[108:109]
	s_ashr_i32 s2, s4, 5
	s_mul_hi_i32 s3, s2, 0x4080
	s_mulk_i32 s2, 0x4080
	v_lshrrev_b32_e32 v27, 6, v0
	s_add_u32 s2, s62, s2
	s_addc_u32 s3, s63, s3
	v_lshlrev_b32_e32 v6, 10, v27
	v_lshl_add_u64 v[4:5], s[2:3], 0, v[108:109]
	v_mov_b32_e32 v7, v109
	v_lshl_add_u64 v[8:9], v[2:3], 0, v[6:7]
	v_lshl_add_u64 v[10:11], v[4:5], 0, v[6:7]
	v_add_u32_e32 v14, 0x3000, v6
	v_add_u32_e32 v16, 0x6000, v6
	v_add_u32_e32 v18, 0x9000, v6
	v_bfe_u32 v119, v0, 6, 2
	v_and_b32_e32 v118, 31, v0
	s_mov_b64 s[62:63], 0xc00
	v_add_u32_e32 v15, 0x15000, v6
	s_mov_b64 s[2:3], 0xc00
	v_lshl_add_u64 v[12:13], v[10:11], 0, s[2:3]
	v_readfirstlane_b32 s4, v15
	s_mov_b32 m0, s4
	s_nop 0
	global_load_lds_dwordx4 v[12:13], off
	v_add_u32_e32 v15, 0x18000, v6
	s_mov_b64 s[2:3], 0x3c00
	v_lshl_add_u64 v[12:13], v[10:11], 0, s[2:3]
	v_readfirstlane_b32 s4, v15
	s_mov_b32 m0, s4
	s_nop 0
	global_load_lds_dwordx4 v[12:13], off
	v_add_u32_e32 v15, 0x1b000, v6
	s_mov_b64 s[2:3], 0x6c00
	v_lshl_add_u64 v[12:13], v[10:11], 0, s[2:3]
	v_readfirstlane_b32 s4, v15
	s_mov_b32 m0, s4
	s_nop 0
	global_load_lds_dwordx4 v[12:13], off
	v_add_u32_e32 v15, 0x1e000, v6
	s_mov_b64 s[2:3], 0x9c00
	v_lshl_add_u64 v[12:13], v[10:11], 0, s[2:3]
	v_readfirstlane_b32 s4, v15
	s_mov_b32 m0, s4
	s_nop 0
	global_load_lds_dwordx4 v[12:13], off
	v_add_u32_e32 v15, 0x21000, v6
	s_mov_b64 s[2:3], 0xcc00
	v_lshl_add_u64 v[12:13], v[10:11], 0, s[2:3]
	v_readfirstlane_b32 s4, v15
	s_mov_b32 m0, s4
	s_nop 0
	global_load_lds_dwordx4 v[12:13], off
	v_or_b32_e32 v12, 0x90, v27
	v_min_u32_e32 v12, 0x91, v12
	v_lshlrev_b32_e32 v12, 10, v12
	v_mov_b32_e32 v13, v109
	s_nop 0
	v_readfirstlane_b32 s4, v12
	v_lshl_add_u64 v[12:13], v[4:5], 0, v[12:13]
	s_mov_b32 s2, 0xfffebc00
	s_mov_b32 s3, -1
	v_lshl_add_u64 v[12:13], v[12:13], 0, s[2:3]
	s_mov_b32 m0, s4
	s_nop 0
	global_load_lds_dwordx4 v[12:13], off
	s_movk_i32 s2, 0xdc00
	s_mov_b32 s3, -1
	v_lshl_add_u64 v[12:13], v[10:11], 0, s[2:3]
	s_mov_b64 s[2:3], 0x12000
	v_lshl_add_u64 v[142:143], v[8:9], 0, s[2:3]
	s_movk_i32 s4, 0x23f
	v_cmp_lt_u32_e32 vcc, s4, v0
	v_add_u32_e32 v15, 0x12000, v6
	s_nop 0
	v_cndmask_b32_e32 v12, v142, v12, vcc
	v_cndmask_b32_e32 v13, v143, v13, vcc
	v_readfirstlane_b32 s4, v15
	s_mov_b32 m0, s4
	s_nop 0
	global_load_lds_dwordx4 v[12:13], off
	v_mov_b32_e32 v15, v6
	v_mov_b32_e32 v12, v8
	v_mov_b32_e32 v13, v9
	v_readfirstlane_b32 s4, v15
	s_mov_b32 m0, s4
	s_nop 0
	global_load_lds_dwordx4 v[12:13], off
	v_add_u32_e32 v15, 0x3000, v6
	s_mov_b64 s[2:3], 0x3000
	v_lshl_add_u64 v[12:13], v[8:9], 0, s[2:3]
	v_readfirstlane_b32 s4, v15
	s_mov_b32 m0, s4
	s_nop 0
	global_load_lds_dwordx4 v[12:13], off
	v_add_u32_e32 v15, 0x6000, v6
	s_mov_b64 s[2:3], 0x6000
	v_lshl_add_u64 v[12:13], v[8:9], 0, s[2:3]
	v_readfirstlane_b32 s4, v15
	s_mov_b32 m0, s4
	s_nop 0
	global_load_lds_dwordx4 v[12:13], off
	v_add_u32_e32 v15, 0x9000, v6
	s_mov_b64 s[2:3], 0x9000
	v_lshl_add_u64 v[12:13], v[8:9], 0, s[2:3]
	v_readfirstlane_b32 s4, v15
	s_mov_b32 m0, s4
	s_nop 0
	global_load_lds_dwordx4 v[12:13], off
	v_add_u32_e32 v15, 0xc000, v6
	s_mov_b64 s[2:3], 0xc000
	v_lshl_add_u64 v[12:13], v[8:9], 0, s[2:3]
	v_readfirstlane_b32 s4, v15
	s_mov_b32 m0, s4
	s_nop 0
	global_load_lds_dwordx4 v[12:13], off
	v_add_u32_e32 v15, 0xf000, v6
	s_mov_b64 s[2:3], 0xf000
	v_lshl_add_u64 v[12:13], v[8:9], 0, s[2:3]
	v_readfirstlane_b32 s4, v15
	s_mov_b32 m0, s4
	s_nop 0
	global_load_lds_dwordx4 v[12:13], off
	s_mov_b32 s2, 0x14400
	s_and_b64 vcc, exec, s[68:69]
	s_cbranch_vccz .Lpx_skip
	v_readfirstlane_b32 s84, v115
	s_cmp_lg_u32 s84, 2
	s_cbranch_scc1 .Lpx_skip
	v_lshlrev_b32_e32 v154, 2, v1
	s_cmp_eq_u32 s78, 0
	s_cbranch_scc1 .Lpx_ld_done
	s_add_u32 s85, s72, 0
	s_lshl_b32 s85, s85, 10
	v_add_u32_e32 v155, s85, v154
	global_load_dword v92, v155, s[60:61]
	s_cmp_ge_u32 1, s78
	s_cbranch_scc1 .Lpx_ld_done
	s_add_u32 s85, s72, 1
	s_lshl_b32 s85, s85, 10
	v_add_u32_e32 v155, s85, v154
	global_load_dword v93, v155, s[60:61]
	s_cmp_ge_u32 2, s78
	s_cbranch_scc1 .Lpx_ld_done
	s_add_u32 s85, s72, 2
	s_lshl_b32 s85, s85, 10
	v_add_u32_e32 v155, s85, v154
	global_load_dword v94, v155, s[60:61]
	s_cmp_ge_u32 3, s78
	s_cbranch_scc1 .Lpx_ld_done
	s_add_u32 s85, s72, 3
	s_lshl_b32 s85, s85, 10
	v_add_u32_e32 v155, s85, v154
	global_load_dword v95, v155, s[60:61]
	s_cmp_ge_u32 4, s78
	s_cbranch_scc1 .Lpx_ld_done
	s_add_u32 s85, s72, 4
	s_lshl_b32 s85, s85, 10
	v_add_u32_e32 v155, s85, v154
	global_load_dword v96, v155, s[60:61]
	s_cmp_ge_u32 5, s78
	s_cbranch_scc1 .Lpx_ld_done
	s_add_u32 s85, s72, 5
	s_lshl_b32 s85, s85, 10
	v_add_u32_e32 v155, s85, v154
	global_load_dword v97, v155, s[60:61]
	s_cmp_ge_u32 6, s78
	s_cbranch_scc1 .Lpx_ld_done
	s_add_u32 s85, s72, 6
	s_lshl_b32 s85, s85, 10
	v_add_u32_e32 v155, s85, v154
	global_load_dword v98, v155, s[60:61]
	s_cmp_ge_u32 7, s78
	s_cbranch_scc1 .Lpx_ld_done
	s_add_u32 s85, s72, 7
	s_lshl_b32 s85, s85, 10
	v_add_u32_e32 v155, s85, v154
	global_load_dword v99, v155, s[60:61]
	s_cmp_ge_u32 8, s78
	s_cbranch_scc1 .Lpx_ld_done
	s_add_u32 s85, s72, 8
	s_lshl_b32 s85, s85, 10
	v_add_u32_e32 v155, s85, v154
	global_load_dword v100, v155, s[60:61]
	s_cmp_ge_u32 9, s78
	s_cbranch_scc1 .Lpx_ld_done
	s_add_u32 s85, s72, 9
	s_lshl_b32 s85, s85, 10
	v_add_u32_e32 v155, s85, v154
	global_load_dword v101, v155, s[60:61]
	s_cmp_ge_u32 10, s78
	s_cbranch_scc1 .Lpx_ld_done
	s_add_u32 s85, s72, 10
	s_lshl_b32 s85, s85, 10
	v_add_u32_e32 v155, s85, v154
	global_load_dword v102, v155, s[60:61]
	s_cmp_ge_u32 11, s78
	s_cbranch_scc1 .Lpx_ld_done
	s_add_u32 s85, s72, 11
	s_lshl_b32 s85, s85, 10
	v_add_u32_e32 v155, s85, v154
	global_load_dword v103, v155, s[60:61]
	s_cmp_ge_u32 12, s78
	s_cbranch_scc1 .Lpx_ld_done
	s_add_u32 s85, s72, 12
	s_lshl_b32 s85, s85, 10
	v_add_u32_e32 v155, s85, v154
	global_load_dword v104, v155, s[60:61]
	s_cmp_ge_u32 13, s78
	s_cbranch_scc1 .Lpx_ld_done
	s_add_u32 s85, s72, 13
	s_lshl_b32 s85, s85, 10
	v_add_u32_e32 v155, s85, v154
	global_load_dword v105, v155, s[60:61]
	s_cmp_ge_u32 14, s78
	s_cbranch_scc1 .Lpx_ld_done
	s_add_u32 s85, s72, 14
	s_lshl_b32 s85, s85, 10
	v_add_u32_e32 v155, s85, v154
	global_load_dword v106, v155, s[60:61]
	s_cmp_ge_u32 15, s78
	s_cbranch_scc1 .Lpx_ld_done
	s_add_u32 s85, s72, 15
	s_lshl_b32 s85, s85, 10
	v_add_u32_e32 v155, s85, v154
	global_load_dword v107, v155, s[60:61]
	s_cmp_ge_u32 16, s78
	s_cbranch_scc1 .Lpx_ld_done
	s_add_u32 s85, s72, 16
	s_lshl_b32 s85, s85, 10
	v_add_u32_e32 v155, s85, v154
	global_load_dword v142, v155, s[60:61]
	s_cmp_ge_u32 17, s78
	s_cbranch_scc1 .Lpx_ld_done
	s_add_u32 s85, s72, 17
	s_lshl_b32 s85, s85, 10
	v_add_u32_e32 v155, s85, v154
	global_load_dword v143, v155, s[60:61]
	s_cmp_ge_u32 18, s78
	s_cbranch_scc1 .Lpx_ld_done
	s_add_u32 s85, s72, 18
	s_lshl_b32 s85, s85, 10
	v_add_u32_e32 v155, s85, v154
	global_load_dword v144, v155, s[60:61]
	s_cmp_ge_u32 19, s78
	s_cbranch_scc1 .Lpx_ld_done
	s_add_u32 s85, s72, 19
	s_lshl_b32 s85, s85, 10
	v_add_u32_e32 v155, s85, v154
	global_load_dword v145, v155, s[60:61]
	s_cmp_ge_u32 20, s78
	s_cbranch_scc1 .Lpx_ld_done
	s_add_u32 s85, s72, 20
	s_lshl_b32 s85, s85, 10
	v_add_u32_e32 v155, s85, v154
	global_load_dword v146, v155, s[60:61]
	s_cmp_ge_u32 21, s78
	s_cbranch_scc1 .Lpx_ld_done
	s_add_u32 s85, s72, 21
	s_lshl_b32 s85, s85, 10
	v_add_u32_e32 v155, s85, v154
	global_load_dword v147, v155, s[60:61]
	s_cmp_ge_u32 22, s78
	s_cbranch_scc1 .Lpx_ld_done
	s_add_u32 s85, s72, 22
	s_lshl_b32 s85, s85, 10
	v_add_u32_e32 v155, s85, v154
	global_load_dword v148, v155, s[60:61]
	s_cmp_ge_u32 23, s78
	s_cbranch_scc1 .Lpx_ld_done
	s_add_u32 s85, s72, 23
	s_lshl_b32 s85, s85, 10
	v_add_u32_e32 v155, s85, v154
	global_load_dword v149, v155, s[60:61]
	s_cmp_ge_u32 24, s78
	s_cbranch_scc1 .Lpx_ld_done
	s_add_u32 s85, s72, 24
	s_lshl_b32 s85, s85, 10
	v_add_u32_e32 v155, s85, v154
	global_load_dword v150, v155, s[60:61]
	s_cmp_ge_u32 25, s78
	s_cbranch_scc1 .Lpx_ld_done
	s_add_u32 s85, s72, 25
	s_lshl_b32 s85, s85, 10
	v_add_u32_e32 v155, s85, v154
	global_load_dword v151, v155, s[60:61]
	s_cmp_ge_u32 26, s78
	s_cbranch_scc1 .Lpx_ld_done
	s_add_u32 s85, s72, 26
	s_lshl_b32 s85, s85, 10
	v_add_u32_e32 v155, s85, v154
	global_load_dword v152, v155, s[60:61]
	s_cmp_ge_u32 27, s78
	s_cbranch_scc1 .Lpx_ld_done
	s_add_u32 s85, s72, 27
	s_lshl_b32 s85, s85, 10
	v_add_u32_e32 v155, s85, v154
	global_load_dword v153, v155, s[60:61]
.Lpx_ld_done:
.Lpx_skip:
	v_mul_u32_u24_e32 v4, 0x4080, v119
	s_and_b64 vcc, exec, s[68:69]
	s_cbranch_vccz .Lw1_n
	v_readfirstlane_b32 s84, v115
	s_cmp_lg_u32 s84, 2
	s_cbranch_scc1 .Lw1_n
	s_cmp_ge_u32 s78, 28
	s_cbranch_scc1 .Lw1_28
	s_cmp_eq_u32 s78, 24
	s_cbranch_scc1 .Lw1_24
	s_cmp_eq_u32 s78, 20
	s_cbranch_scc1 .Lw1_20
	s_branch .Lw1_n
.Lw1_28:
	s_waitcnt vmcnt(34)
	s_branch .Lw1_e
.Lw1_24:
	s_waitcnt vmcnt(30)
	s_branch .Lw1_e
.Lw1_20:
	s_waitcnt vmcnt(26)
	s_branch .Lw1_e
.Lw1_n:
	s_waitcnt vmcnt(6)
.Lw1_e:
	v_add3_u32 v5, v108, v4, s2
	v_lshl_or_b32 v4, v118, 2, v4
	s_mov_b64 s[2:3], 0x14280
	s_waitcnt lgkmcnt(0)
	s_barrier
	v_add_u32_e32 v4, 0x18400, v4
	v_lshl_add_u64 v[2:3], v[2:3], 0, s[2:3]
	ds_read_b128 v[88:91], v5
	ds_read_b128 v[84:87], v5 offset:1024
	ds_read_b128 v[80:83], v5 offset:2048
	ds_read_b128 v[76:79], v5 offset:3072
	ds_read_b128 v[72:75], v5 offset:4096
	ds_read_b128 v[68:71], v5 offset:5120
	ds_read_b128 v[64:67], v5 offset:6144
	ds_read_b128 v[60:63], v5 offset:7168
	ds_read_b128 v[56:59], v5 offset:8192
	ds_read_b128 v[52:55], v5 offset:9216
	ds_read_b128 v[48:51], v5 offset:10240
	ds_read_b128 v[44:47], v5 offset:11264
	ds_read_b128 v[40:43], v5 offset:12288
	ds_read_b128 v[36:39], v5 offset:13312
	ds_read_b128 v[32:35], v5 offset:14336
	ds_read_b128 v[28:31], v5 offset:15360
	ds_read_b32 v116, v4
	s_waitcnt lgkmcnt(0)
	v_lshl_add_u64 v[4:5], v[2:3], 0, v[6:7]
	v_add_u32_e32 v7, 0x14280, v6
	s_barrier
	v_readfirstlane_b32 s2, v7
	v_add_u32_e32 v7, 0x17280, v6
	s_mov_b32 m0, s2
	v_mov_b32_e32 v15, v109
	v_readfirstlane_b32 s2, v7
	v_add_u32_e32 v7, 0x1a280, v6
	global_load_lds_dwordx4 v[4:5], off
	v_lshl_add_u64 v[4:5], v[2:3], 0, v[14:15]
	s_mov_b32 m0, s2
	v_mov_b32_e32 v17, v109
	v_readfirstlane_b32 s2, v7
	v_add_u32_e32 v7, 0x1d280, v6
	global_load_lds_dwordx4 v[4:5], off
	v_lshl_add_u64 v[4:5], v[2:3], 0, v[16:17]
	s_mov_b32 m0, s2
	v_mov_b32_e32 v19, v109
	v_readfirstlane_b32 s2, v7
	global_load_lds_dwordx4 v[4:5], off
	v_lshl_add_u64 v[4:5], v[2:3], 0, v[18:19]
	s_mov_b32 m0, s2
	v_bfe_u32 v117, v0, 5, 1
	global_load_lds_dwordx4 v[4:5], off
	v_or_b32_e32 v4, 0xc000, v6
	v_add_u32_e32 v6, 0x20280, v6
	v_mov_b32_e32 v5, v109
	v_readfirstlane_b32 s2, v6
	v_lshl_add_u64 v[4:5], v[2:3], 0, v[4:5]
	s_mov_b32 m0, s2
	v_add_u32_e32 v131, 33, v115
	global_load_lds_dwordx4 v[4:5], off
	v_min_u32_e32 v4, 4, v27
	v_lshlrev_b32_e32 v6, 10, v4
	v_add_u32_e32 v4, 0xf000, v6
	v_mov_b32_e32 v5, v109
	v_lshl_add_u64 v[2:3], v[2:3], 0, v[4:5]
	v_add_u32_e32 v4, 0x23280, v6
	s_movk_i32 s73, 0x4080
	v_readfirstlane_b32 s2, v4
	s_mov_b32 m0, s2
	v_mov_b32_e32 v18, 0x7f800000
	global_load_lds_dwordx4 v[2:3], off
	v_mul_u32_u24_e32 v2, 0x4080, v115
	v_lshl_or_b32 v2, v117, 4, v2
	v_add_u32_e32 v132, 0x4000, v2
	v_lshl_or_b32 v2, s59, 2, v119
	v_sub_u32_e32 v134, v2, v115
	v_add_u32_e32 v2, s72, v131
	v_ashrrev_i32_e32 v3, 31, v2
	v_lshlrev_b64 v[2:3], 10, v[2:3]
	v_lshl_or_b32 v2, v1, 2, v2
	v_lshl_add_u64 v[110:111], s[0:1], 0, v[108:109]
	v_cmp_gt_i32_e64 s[0:1], s78, v131
	v_mad_u32_u24 v133, v115, s73, v108
	v_lshl_add_u64 v[112:113], s[60:61], 0, v[2:3]
	s_mov_b64 s[60:61], -1
	v_mov_b32_e32 v135, 0x4080
	v_mov_b32_e32 v136, 0xff800000
	v_mov_b32_e32 v137, 0
	s_mov_b32 s81, s79
	v_mov_b32_e32 v1, v18
	v_mov_b32_e32 v20, v18
	v_mov_b32_e32 v19, v18
	v_mov_b32_e32 v24, v18
	v_mov_b32_e32 v23, v18
	v_mov_b32_e32 v22, v18
	v_mov_b32_e32 v21, v18
	v_mov_b32_e32 v26, v18
	v_mov_b32_e32 v25, v18
	s_and_b64 vcc, exec, s[68:69]
	s_cbranch_vccz .Lce_skip
	v_readfirstlane_b32 s84, v115
	s_cmp_lg_u32 s84, 2
	s_cbranch_scc1 .Lce_skip
	s_waitcnt vmcnt(6)
	v_mov_b32_e32 v156, 0
	s_cmp_eq_u32 s78, 0
	s_cbranch_scc1 .Lce_sum_done
	v_add_f32_e32 v156, v156, v92
	s_cmp_ge_u32 1, s78
	s_cbranch_scc1 .Lce_sum_done
	v_add_f32_e32 v156, v156, v93
	s_cmp_ge_u32 2, s78
	s_cbranch_scc1 .Lce_sum_done
	v_add_f32_e32 v156, v156, v94
	s_cmp_ge_u32 3, s78
	s_cbranch_scc1 .Lce_sum_done
	v_add_f32_e32 v156, v156, v95
	s_cmp_ge_u32 4, s78
	s_cbranch_scc1 .Lce_sum_done
	v_add_f32_e32 v156, v156, v96
	s_cmp_ge_u32 5, s78
	s_cbranch_scc1 .Lce_sum_done
	v_add_f32_e32 v156, v156, v97
	s_cmp_ge_u32 6, s78
	s_cbranch_scc1 .Lce_sum_done
	v_add_f32_e32 v156, v156, v98
	s_cmp_ge_u32 7, s78
	s_cbranch_scc1 .Lce_sum_done
	v_add_f32_e32 v156, v156, v99
	s_cmp_ge_u32 8, s78
	s_cbranch_scc1 .Lce_sum_done
	v_add_f32_e32 v156, v156, v100
	s_cmp_ge_u32 9, s78
	s_cbranch_scc1 .Lce_sum_done
	v_add_f32_e32 v156, v156, v101
	s_cmp_ge_u32 10, s78
	s_cbranch_scc1 .Lce_sum_done
	v_add_f32_e32 v156, v156, v102
	s_cmp_ge_u32 11, s78
	s_cbranch_scc1 .Lce_sum_done
	v_add_f32_e32 v156, v156, v103
	s_cmp_ge_u32 12, s78
	s_cbranch_scc1 .Lce_sum_done
	v_add_f32_e32 v156, v156, v104
	s_cmp_ge_u32 13, s78
	s_cbranch_scc1 .Lce_sum_done
	v_add_f32_e32 v156, v156, v105
	s_cmp_ge_u32 14, s78
	s_cbranch_scc1 .Lce_sum_done
	v_add_f32_e32 v156, v156, v106
	s_cmp_ge_u32 15, s78
	s_cbranch_scc1 .Lce_sum_done
	v_add_f32_e32 v156, v156, v107
	s_cmp_ge_u32 16, s78
	s_cbranch_scc1 .Lce_sum_done
	v_add_f32_e32 v156, v156, v142
	s_cmp_ge_u32 17, s78
	s_cbranch_scc1 .Lce_sum_done
	v_add_f32_e32 v156, v156, v143
	s_cmp_ge_u32 18, s78
	s_cbranch_scc1 .Lce_sum_done
	v_add_f32_e32 v156, v156, v144
	s_cmp_ge_u32 19, s78
	s_cbranch_scc1 .Lce_sum_done
	v_add_f32_e32 v156, v156, v145
	s_cmp_ge_u32 20, s78
	s_cbranch_scc1 .Lce_sum_done
	v_add_f32_e32 v156, v156, v146
	s_cmp_ge_u32 21, s78
	s_cbranch_scc1 .Lce_sum_done
	v_add_f32_e32 v156, v156, v147
	s_cmp_ge_u32 22, s78
	s_cbranch_scc1 .Lce_sum_done
	v_add_f32_e32 v156, v156, v148
	s_cmp_ge_u32 23, s78
	s_cbranch_scc1 .Lce_sum_done
	v_add_f32_e32 v156, v156, v149
	s_cmp_ge_u32 24, s78
	s_cbranch_scc1 .Lce_sum_done
	v_add_f32_e32 v156, v156, v150
	s_cmp_ge_u32 25, s78
	s_cbranch_scc1 .Lce_sum_done
	v_add_f32_e32 v156, v156, v151
	s_cmp_ge_u32 26, s78
	s_cbranch_scc1 .Lce_sum_done
	v_add_f32_e32 v156, v156, v152
	s_cmp_ge_u32 27, s78
	s_cbranch_scc1 .Lce_sum_done
	v_add_f32_e32 v156, v156, v153
	s_cmp_le_u32 s78, 28
	s_cbranch_scc1 .Lce_sum_done
	s_mov_b32 s86, 28
.Lce_rare:
	s_add_u32 s85, s72, s86
	s_lshl_b32 s85, s85, 10
	v_add_u32_e32 v155, s85, v154
	global_load_dword v157, v155, s[60:61]
	s_add_u32 s86, s86, 1
	s_waitcnt vmcnt(0)
	v_add_f32_e32 v156, v156, v157
	s_cmp_lt_u32 s86, s78
	s_cbranch_scc1 .Lce_rare
.Lce_sum_done:
	s_bfe_u32 s88, s77, 0x80008
	s_cmp_lg_u32 s59, 0
	s_cbranch_scc1 .Lce_nostore
	v_lshl_or_b32 v157, s88, 10, v154
	global_store_dword v157, v156, s[64:65]
.Lce_nostore:
	v_cvt_f32_i32_e32 v157, s58
	v_mov_b32_e32 v158, 0x25400
	v_add_u32_e32 v158, v158, v154
	v_div_scale_f32 v92, s[86:87], v157, v157, v156
	v_rcp_f32_e32 v93, v92
	v_div_scale_f32 v94, vcc, v156, v157, v156
	v_fma_f32 v95, -v92, v93, 1.0
	v_fmac_f32_e32 v93, v95, v93
	v_mul_f32_e32 v95, v94, v93
	v_fma_f32 v96, -v92, v95, v94
	v_fmac_f32_e32 v95, v96, v93
	v_fma_f32 v92, -v92, v95, v94
	v_div_fmas_f32 v92, v92, v93, v95
	v_div_fixup_f32 v156, v92, v157, v156
	v_mul_f32_e32 v157, v156, v156
	ds_write_b32 v158, v156
	v_cmp_eq_u32_e32 vcc, 0, v114
	v_mov_b32_dpp v157, v157 quad_perm:[1,0,3,2] row_mask:0xf bank_mask:0xf bound_ctrl:1
	v_fmac_f32_e32 v157, v156, v156
	s_nop 1
	v_add_f32_dpp v156, v157, v157 quad_perm:[2,3,0,1] row_mask:0xf bank_mask:0xf bound_ctrl:1
	s_nop 1
	v_add_f32_dpp v156, v156, v156 row_half_mirror row_mask:0xf bank_mask:0xf bound_ctrl:1
	s_nop 1
	v_add_f32_dpp v156, v156, v156 row_mirror row_mask:0xf bank_mask:0xf bound_ctrl:1
	s_nop 0
	v_readlane_b32 s88, v156, 0
	v_readlane_b32 s90, v156, 16
	v_readlane_b32 s89, v156, 32
	v_readlane_b32 s91, v156, 48
	s_and_saveexec_b64 s[84:85], vcc
	s_cbranch_execz .Lce_cdone
	v_mov_b32_e32 v156, 0x25810
	v_lshl_add_u32 v158, v27, 2, v156
	v_mov_b32_e32 v156, s90
	v_mov_b32_e32 v157, s91
	v_pk_add_f32 v[156:157], s[88:89], v[156:157]
	s_nop 0
	v_add_f32_e32 v156, v156, v157
	ds_write_b32 v158, v156

.LBB1_21:
	s_waitcnt vmcnt(0)
	s_mov_b64 s[60:61], 0
	s_andn2_b64 vcc, exec, s[60:61]
	s_cbranch_vccnz .LBB1_5
	s_waitcnt vmcnt(0)
	v_sub_u32_e32 v142, s78, v115
	v_cmp_lt_i32_e64 s[36:37], 0, v142
	v_cmp_lt_i32_e64 s[38:39], 3, v142
	v_cmp_lt_i32_e64 s[40:41], 6, v142
	v_cmp_lt_i32_e64 s[42:43], 9, v142
	v_cmp_lt_i32_e64 s[44:45], 12, v142
	v_cmp_lt_i32_e64 s[46:47], 15, v142
	v_cmp_lt_i32_e64 s[48:49], 18, v142
	v_cmp_lt_i32_e64 s[50:51], 21, v142
	v_cmp_lt_i32_e64 s[52:53], 24, v142
	v_cmp_lt_i32_e64 s[54:55], 27, v142
	v_cmp_lt_i32_e64 s[56:57], 30, v142
	v_mov_b32_e32 v2, v120
	v_mov_b32_e32 v3, v121
	v_add_f32_e32 v2, 0, v2
	v_cndmask_b32_e64 v2, 0, v2, s[36:37]
	v_cndmask_b32_e64 v3, 0, v3, s[38:39]
	v_add_f32_e32 v2, v2, v3
	v_mov_b32_e32 v3, v122
	s_nop 0
	v_cndmask_b32_e64 v3, 0, v3, s[40:41]
	v_add_f32_e32 v2, v2, v3
	v_mov_b32_e32 v3, v123
	s_nop 0
	v_cndmask_b32_e64 v3, 0, v3, s[42:43]
	v_add_f32_e32 v2, v2, v3
	v_mov_b32_e32 v3, v124
	s_nop 0
	v_cndmask_b32_e64 v3, 0, v3, s[44:45]
	v_add_f32_e32 v2, v2, v3
	v_mov_b32_e32 v3, v125
	s_nop 0
	v_cndmask_b32_e64 v3, 0, v3, s[46:47]
	v_add_f32_e32 v2, v2, v3
	v_mov_b32_e32 v3, v126
	s_nop 0
	v_cndmask_b32_e64 v3, 0, v3, s[48:49]
	v_add_f32_e32 v2, v2, v3
	v_mov_b32_e32 v3, v127
	s_nop 0
	v_cndmask_b32_e64 v3, 0, v3, s[50:51]
	v_add_f32_e32 v2, v2, v3
	v_mov_b32_e32 v3, v128
	s_nop 0
	v_cndmask_b32_e64 v3, 0, v3, s[52:53]
	v_add_f32_e32 v2, v2, v3
	v_mov_b32_e32 v3, v129
	s_nop 0
	v_cndmask_b32_e64 v3, 0, v3, s[54:55]
	v_add_f32_e32 v2, v2, v3
	v_mov_b32_e32 v3, v130
	s_nop 0
	v_cndmask_b32_e64 v3, 0, v3, s[56:57]
	v_add_f32_e32 v137, v2, v3
	s_and_saveexec_b64 s[60:61], s[0:1]
	s_cbranch_execz .LBB1_4
	s_mov_b64 s[72:73], 0
	v_mov_b64_e32 v[2:3], v[112:113]
	v_mov_b32_e32 v4, v131

.LBB1_26:
	s_branch .Lt_nw
	v_mov_b32_e32 v2, 0x24800
	v_lshl_add_u32 v2, v0, 2, v2
	ds_write_b32 v2, v137
